# stagger: half the workgroups (block bit 3) start the three residual GEMM phases 3 x s_sleep 127 late so HBM-bound epilogues overlap the other half K-loops
# speedup vs baseline: 1.0013x; 1.0013x over previous
; #define PG8_STAGE(bufoff, gbase, voff) do { _Pragma("unroll") for (int _i = 0; _i < 2; ++_i) { const char* gb_ = (const char*)(gbase) + _i * rstep; asm volatile("" : "+s"(gb_));   \
;         __builtin_amdgcn_global_load_lds((const unsigned*)(gb_ + (voff)), (LAS unsigned*)(lds + (bufoff) + ldsw + _i * 8192), 16, 0, 0); } } while (0)
; #define PG8_BAR __builtin_amdgcn_s_barrier()
; template <class Epi, class Sched, bool ALIGN_EPI = true, bool SP2 = true, bool I8 = false, bool F8 = false>
; __device__ __forceinline__ void gemm_phase(LAS unsigned char* lds, const int K, const Sched& S, const Epi& E, const int wave) {
;     ...
;     const int tid = tid_, wid = __builtin_amdgcn_readfirstlane(tid >> 6), lane = tid & 63, wr = wid >> 2, wc = wid & 3, fr = lane & 15, fq = lane >> 4;
;     const int nt = K / BK;
;     unsigned voffA, voffB;
;     { int R, C; stage_rc(tid * 16, R, C); const int Rb = Epi::PERM ? ((R & ~31) + perm32(R & 31)) : R;
;       voffA = (unsigned)(R * K + C) * 2u; voffB = (unsigned)(Rb * K + C) * 2u; }
;     const size_t rstep = (size_t)64 * K * 2;
;     const size_t kstep = (size_t)(BK * 2);
;     const size_t hstep = (size_t)HALF * K * 2;
;     const unsigned ldsw = (unsigned)wid * 1024u;
;     const int aoff = lds_byte(wr * 64 + fr, fq * 8), boff = lds_byte(wc * 32 + fr, fq * 8);
;     ...
;     Unit cur, nxt; int ui = 0;
;     if (!S.next(0, cur)) return;
;     acc_t acc[2][2][4][2];
; #pragma unroll
;     for (int a = 0; a < 2; ++a)
; #pragma unroll
;         for (int b = 0; b < 2; ++b)
; #pragma unroll
;             for (int m = 0; m < 4; ++m)
; #pragma unroll
;                 for (int n = 0; n < 2; ++n) acc[a][b][m][n] = (acc_t){0, 0, 0, 0};
;     bf16x8 At[4][2], B0[2][2], B1[2][2];
;     const char* cA = cur.a; const char* cB = cur.b;
;     if constexpr (SP2) {
;         PG8_STAGE(PG8_SB(0, 0), cB, voffB); PG8_STAGE(PG8_SB(0, 1), cB + hstep, voffB); PG8_STAGE(PG8_SA(0, 0), cA, voffA); PG8_STAGE(PG8_SA(0, 1), cA + hstep, voffA);
;         if (wr == 1) PG8_BAR;
.LBB0_1073:
	s_andn2_b64 vcc, exec, s[0:1]
	s_cbranch_vccnz .LBB0_1109
	s_bitcmp1_b32 s28, 3
	s_cbranch_scc0 .Lstg_wo_done
	s_movk_i32 s6, 3
.Lstg_wo_loop:
	s_sleep 127
	s_add_i32 s6, s6, -1
	s_cmp_lg_u32 s6, 0
	s_cbranch_scc1 .Lstg_wo_loop
.Lstg_wo_done:
	v_bfe_i32 v3, v0, 27, 1
	v_lshlrev_b32_e32 v1, 4, v0
	v_lshrrev_b32_e32 v3, 22, v3
	v_add_u32_e32 v3, v1, v3
	v_and_b32_e32 v3, 0xfffffc00, v3
	v_sub_u32_e32 v1, v1, v3
	v_ashrrev_i32_e32 v2, 31, v0
	v_lshrrev_b32_e32 v3, 4, v1
	v_lshrrev_b32_e32 v2, 26, v2
	v_bitop3_b32 v1, v3, v1, 32 bitop3:0x6c
	v_add_u32_e32 v2, v0, v2
	v_ashrrev_i32_e32 v4, 31, v1
	v_ashrrev_i32_e32 v2, 6, v2
	v_lshrrev_b32_e32 v4, 26, v4
	v_lshlrev_b32_e32 v3, 3, v2
	v_add_u32_e32 v4, v1, v4
	v_and_b32_e32 v3, -16, v3
	v_ashrrev_i32_e32 v5, 6, v4
	v_and_b32_e32 v4, 0xc0, v4
	v_add_u32_e32 v3, v5, v3
	v_sub_u32_e32 v1, v1, v4
	s_ashr_i32 s6, s3, 6
	v_lshlrev_b32_e32 v2, 5, v2
	v_ashrrev_i16_sdwa v1, v248, sext(v1) dst_sel:DWORD dst_unused:UNUSED_PAD src0_sel:DWORD src1_sel:BYTE_0
	v_lshlrev_b32_e32 v4, 1, v3
	v_lshrrev_b32_e32 v6, 2, v3
	v_and_b32_e32 v5, 3, v5
	s_mov_b32 s0, 0x1fffe0
	v_and_b32_e32 v2, 32, v2
	v_bfe_i32 v1, v1, 0, 16
	v_and_b32_e32 v4, 24, v4
	v_and_b32_e32 v6, 4, v6
	v_and_or_b32 v5, v3, s0, v5
	s_lshl_b32 s34, s6, 10
	v_or3_b32 v4, v5, v6, v4
	v_add_lshl_u32 v1, v2, v1, 1
	s_add_i32 s35, s34, 0
	s_mov_b64 s[0:1], s[22:23]
	s_ashr_i32 s7, s3, 8
	v_lshl_add_u32 v112, v4, 11, v1
	s_add_i32 m0, s35, 0x10000
	v_lshl_add_u32 v154, v3, 11, v1
	global_load_lds_dwordx4 v112, s[0:1]
	s_add_u32 s0, s22, 0x20000
	s_addc_u32 s1, s23, 0
	s_add_i32 m0, s35, 0x12000
	s_nop 0
	global_load_lds_dwordx4 v112, s[0:1]
	s_add_u32 s0, s22, 0x40000
	s_addc_u32 s1, s23, 0
	s_add_i32 m0, s35, 0x14000
	s_nop 0
	global_load_lds_dwordx4 v112, s[0:1]
	s_add_u32 s0, s22, 0x60000
	s_addc_u32 s1, s23, 0
	s_add_i32 m0, s35, 0x16000
	s_nop 0
	global_load_lds_dwordx4 v112, s[0:1]
	s_mov_b64 s[0:1], s[20:21]
	s_mov_b32 m0, s35
	s_nop 0
	global_load_lds_dwordx4 v154, s[0:1]
	s_add_u32 s0, s20, 0x20000
	s_addc_u32 s1, s21, 0
	s_add_i32 s36, s35, 0x2000
	s_mov_b32 m0, s36
	s_nop 0
	global_load_lds_dwordx4 v154, s[0:1]
	s_add_u32 s0, s20, 0x40000
	s_addc_u32 s1, s21, 0
	s_add_i32 s37, s35, 0x4000
	s_mov_b32 m0, s37
	s_nop 0
	global_load_lds_dwordx4 v154, s[0:1]
	s_add_u32 s0, s20, 0x60000
	s_addc_u32 s1, s21, 0
	s_add_i32 s38, s35, 0x6000
	s_mov_b32 m0, s38
	s_cmp_eq_u32 s7, 1
	global_load_lds_dwordx4 v154, s[0:1]
	s_cselect_b64 s[0:1], -1, 0
	s_cmp_lg_u32 s7, 1
	s_cbranch_scc1 .LBB0_1076
	s_barrier

; __device__ __forceinline__ int fresh_tid(int wave) { return wave * 64 + fresh_lane(); }
; #define PG8_STAGE(bufoff, gbase, voff) do { _Pragma("unroll") for (int _i = 0; _i < 2; ++_i) { const char* gb_ = (const char*)(gbase) + _i * rstep; asm volatile("" : "+s"(gb_));   \
;         __builtin_amdgcn_global_load_lds((const unsigned*)(gb_ + (voff)), (LAS unsigned*)(lds + (bufoff) + ldsw + _i * 8192), 16, 0, 0); } } while (0)
; #define PG8_BAR __builtin_amdgcn_s_barrier()
; template <class Epi, class Sched, bool ALIGN_EPI = true, bool SP2 = true, bool I8 = false, bool F8 = false>
; __device__ __forceinline__ void gemm_phase(LAS unsigned char* lds, const int K, const Sched& S, const Epi& E, const int wave) {
;     ...
;     int tid_ = fresh_tid(wave); asm volatile("" : "+v"(tid_));
;     const int tid = tid_, wid = __builtin_amdgcn_readfirstlane(tid >> 6), lane = tid & 63, wr = wid >> 2, wc = wid & 3, fr = lane & 15, fq = lane >> 4;
;     const int nt = K / BK;
;     unsigned voffA, voffB;
;     { int R, C; stage_rc(tid * 16, R, C); const int Rb = Epi::PERM ? ((R & ~31) + perm32(R & 31)) : R;
;       voffA = (unsigned)(R * K + C) * 2u; voffB = (unsigned)(Rb * K + C) * 2u; }
;     const size_t rstep = (size_t)64 * K * 2;
;     const size_t kstep = (size_t)(BK * 2);
;     const size_t hstep = (size_t)HALF * K * 2;
;     const unsigned ldsw = (unsigned)wid * 1024u;
;     const int aoff = lds_byte(wr * 64 + fr, fq * 8), boff = lds_byte(wc * 32 + fr, fq * 8);
;     ...
;     Unit cur, nxt; int ui = 0;
;     if (!S.next(0, cur)) return;
;     acc_t acc[2][2][4][2];
; #pragma unroll
;     for (int a = 0; a < 2; ++a)
; #pragma unroll
;         for (int b = 0; b < 2; ++b)
; #pragma unroll
;             for (int m = 0; m < 4; ++m)
; #pragma unroll
;                 for (int n = 0; n < 2; ++n) acc[a][b][m][n] = (acc_t){0, 0, 0, 0};
;     bf16x8 At[4][2], B0[2][2], B1[2][2];
;     const char* cA = cur.a; const char* cB = cur.b;
;     if constexpr (SP2) {
;         PG8_STAGE(PG8_SB(0, 0), cB, voffB); PG8_STAGE(PG8_SB(0, 1), cB + hstep, voffB); PG8_STAGE(PG8_SA(0, 0), cA, voffA); PG8_STAGE(PG8_SA(0, 1), cA + hstep, voffA);
;         if (wr == 1) PG8_BAR;
;         PG8_WAIT_V(2); PG8_BAR;
;         PG8_STAGE(PG8_SB(1, 0), cB + kstep, voffB); PG8_STAGE(PG8_SA(1, 0), cA + kstep, voffA); PG8_STAGE(PG8_SB(1, 1), cB + hstep + kstep, voffB);
;         PG8_WAIT_V(6); PG8_BAR;
.LBB0_1287:
	s_andn2_b64 vcc, exec, s[0:1]
	s_cbranch_vccnz .LBB0_1323
	s_bitcmp1_b32 s28, 3
	s_cbranch_scc0 .Lstg_xo_done
	s_movk_i32 s2, 3
.Lstg_xo_loop:
	s_sleep 127
	s_add_i32 s2, s2, -1
	s_cmp_lg_u32 s2, 0
	s_cbranch_scc1 .Lstg_xo_loop
.Lstg_xo_done:
	v_bfe_i32 v3, v0, 27, 1
	v_lshlrev_b32_e32 v1, 4, v0
	v_lshrrev_b32_e32 v3, 22, v3
	v_add_u32_e32 v3, v1, v3
	v_and_b32_e32 v3, 0xfffffc00, v3
	v_sub_u32_e32 v1, v1, v3
	v_ashrrev_i32_e32 v2, 31, v0
	v_lshrrev_b32_e32 v3, 4, v1
	v_lshrrev_b32_e32 v2, 26, v2
	v_bitop3_b32 v1, v3, v1, 32 bitop3:0x6c
	v_add_u32_e32 v2, v0, v2
	v_ashrrev_i32_e32 v4, 31, v1
	v_ashrrev_i32_e32 v2, 6, v2
	v_lshrrev_b32_e32 v4, 26, v4
	v_lshlrev_b32_e32 v3, 3, v2
	v_add_u32_e32 v4, v1, v4
	v_and_b32_e32 v3, -16, v3
	v_ashrrev_i32_e32 v5, 6, v4
	v_and_b32_e32 v4, 0xc0, v4
	v_add_u32_e32 v3, v5, v3
	v_sub_u32_e32 v1, v1, v4
	s_ashr_i32 s2, s6, 6
	v_lshlrev_b32_e32 v2, 5, v2
	v_ashrrev_i16_sdwa v1, v248, sext(v1) dst_sel:DWORD dst_unused:UNUSED_PAD src0_sel:DWORD src1_sel:BYTE_0
	v_lshlrev_b32_e32 v4, 1, v3
	v_lshrrev_b32_e32 v6, 2, v3
	v_and_b32_e32 v5, 3, v5
	s_mov_b32 s0, 0x3fffe0
	v_and_b32_e32 v2, 32, v2
	v_bfe_i32 v1, v1, 0, 16
	v_and_b32_e32 v4, 24, v4
	v_and_b32_e32 v6, 4, v6
	v_and_or_b32 v5, v3, s0, v5
	s_lshl_b32 s34, s2, 10
	v_or3_b32 v4, v5, v6, v4
	v_add_lshl_u32 v1, v2, v1, 1
	s_add_i32 s35, s34, 0
	s_mov_b64 s[0:1], s[22:23]
	s_ashr_i32 s3, s6, 8
	v_lshl_add_u32 v112, v4, 10, v1
	s_add_i32 m0, s35, 0x10000
	v_lshl_add_u32 v154, v3, 10, v1
	global_load_lds_dwordx4 v112, s[0:1]
	s_add_u32 s0, s22, 0x10000
	s_addc_u32 s1, s23, 0
	s_add_i32 m0, s35, 0x12000
	s_nop 0
	global_load_lds_dwordx4 v112, s[0:1]
	s_add_u32 s0, s22, 0x20000
	s_addc_u32 s1, s23, 0
	s_add_i32 m0, s35, 0x14000
	s_nop 0
	global_load_lds_dwordx4 v112, s[0:1]
	s_add_u32 s0, s22, 0x30000
	s_addc_u32 s1, s23, 0
	s_add_i32 m0, s35, 0x16000
	s_nop 0
	global_load_lds_dwordx4 v112, s[0:1]
	s_mov_b64 s[0:1], s[20:21]
	s_mov_b32 m0, s35
	s_nop 0
	global_load_lds_dwordx4 v154, s[0:1]
	s_add_u32 s0, s20, 0x10000
	s_addc_u32 s1, s21, 0
	s_add_i32 s36, s35, 0x2000
	s_mov_b32 m0, s36
	s_nop 0
	global_load_lds_dwordx4 v154, s[0:1]
	s_add_u32 s0, s20, 0x20000
	s_addc_u32 s1, s21, 0
	s_add_i32 s37, s35, 0x4000
	s_mov_b32 m0, s37
	s_nop 0
	global_load_lds_dwordx4 v154, s[0:1]
	s_add_u32 s0, s20, 0x30000
	s_addc_u32 s1, s21, 0
	s_add_i32 s38, s35, 0x6000
	s_mov_b32 m0, s38
	s_cmp_eq_u32 s3, 1
	global_load_lds_dwordx4 v154, s[0:1]
	s_cselect_b64 s[0:1], -1, 0
	s_cmp_lg_u32 s3, 1
	s_cbranch_scc1 .LBB0_1290
	s_barrier

; __device__ __forceinline__ int fresh_tid(int wave) { return wave * 64 + fresh_lane(); }
; #define PG8_STAGE(bufoff, gbase, voff) do { _Pragma("unroll") for (int _i = 0; _i < 2; ++_i) { const char* gb_ = (const char*)(gbase) + _i * rstep; asm volatile("" : "+s"(gb_));   \
;         __builtin_amdgcn_global_load_lds((const unsigned*)(gb_ + (voff)), (LAS unsigned*)(lds + (bufoff) + ldsw + _i * 8192), 16, 0, 0); } } while (0)
; #define PG8_BAR __builtin_amdgcn_s_barrier()
; template <class Epi, class Sched, bool ALIGN_EPI = true, bool SP2 = true, bool I8 = false, bool F8 = false>
; __device__ __forceinline__ void gemm_phase(LAS unsigned char* lds, const int K, const Sched& S, const Epi& E, const int wave) {
;     ...
;     int tid_ = fresh_tid(wave); asm volatile("" : "+v"(tid_));
;     const int tid = tid_, wid = __builtin_amdgcn_readfirstlane(tid >> 6), lane = tid & 63, wr = wid >> 2, wc = wid & 3, fr = lane & 15, fq = lane >> 4;
;     const int nt = K / BK;
;     unsigned voffA, voffB;
;     { int R, C; stage_rc(tid * 16, R, C); const int Rb = Epi::PERM ? ((R & ~31) + perm32(R & 31)) : R;
;       voffA = (unsigned)(R * K + C) * 2u; voffB = (unsigned)(Rb * K + C) * 2u; }
;     const size_t rstep = (size_t)64 * K * 2;
;     const size_t kstep = (size_t)(BK * 2);
;     const size_t hstep = (size_t)HALF * K * 2;
;     const unsigned ldsw = (unsigned)wid * 1024u;
;     const int aoff = lds_byte(wr * 64 + fr, fq * 8), boff = lds_byte(wc * 32 + fr, fq * 8);
;     ...
;     Unit cur, nxt; int ui = 0;
;     if (!S.next(0, cur)) return;
;     acc_t acc[2][2][4][2];
; #pragma unroll
;     for (int a = 0; a < 2; ++a)
; #pragma unroll
;         for (int b = 0; b < 2; ++b)
; #pragma unroll
;             for (int m = 0; m < 4; ++m)
; #pragma unroll
;                 for (int n = 0; n < 2; ++n) acc[a][b][m][n] = (acc_t){0, 0, 0, 0};
;     bf16x8 At[4][2], B0[2][2], B1[2][2];
;     const char* cA = cur.a; const char* cB = cur.b;
;     if constexpr (SP2) {
;         PG8_STAGE(PG8_SB(0, 0), cB, voffB); PG8_STAGE(PG8_SB(0, 1), cB + hstep, voffB); PG8_STAGE(PG8_SA(0, 0), cA, voffA); PG8_STAGE(PG8_SA(0, 1), cA + hstep, voffA);
;         if (wr == 1) PG8_BAR;
;         PG8_WAIT_V(2); PG8_BAR;
;         PG8_STAGE(PG8_SB(1, 0), cB + kstep, voffB); PG8_STAGE(PG8_SA(1, 0), cA + kstep, voffA); PG8_STAGE(PG8_SB(1, 1), cB + hstep + kstep, voffB);
;         PG8_WAIT_V(6); PG8_BAR;
.LBB0_1824:
	s_andn2_b64 vcc, exec, s[4:5]
	s_cbranch_vccnz .LBB0_1860
	s_bitcmp1_b32 s24, 3
	s_cbranch_scc0 .Lstg_dd_done
	s_movk_i32 s4, 3
.Lstg_dd_loop:
	s_sleep 127
	s_add_i32 s4, s4, -1
	s_cmp_lg_u32 s4, 0
	s_cbranch_scc1 .Lstg_dd_loop
.Lstg_dd_done:
	v_bfe_i32 v3, v0, 27, 1
	v_lshlrev_b32_e32 v1, 4, v0
	v_lshrrev_b32_e32 v3, 22, v3
	v_add_u32_e32 v3, v1, v3
	v_and_b32_e32 v3, 0xfffffc00, v3
	v_sub_u32_e32 v1, v1, v3
	v_lshrrev_b32_e32 v3, 4, v1
	v_ashrrev_i32_e32 v2, 31, v0
	v_bitop3_b32 v1, v3, v1, 32 bitop3:0x6c
	v_lshrrev_b32_e32 v2, 26, v2
	v_ashrrev_i32_e32 v4, 31, v1
	v_add_u32_e32 v2, v0, v2
	v_lshrrev_b32_e32 v4, 26, v4
	v_ashrrev_i32_e32 v2, 6, v2
	v_add_u32_e32 v4, v1, v4
	v_lshlrev_b32_e32 v3, 3, v2
	v_ashrrev_i32_e32 v5, 6, v4
	v_and_b32_e32 v4, 0xc0, v4
	v_and_b32_e32 v3, -16, v3
	v_lshlrev_b32_e32 v2, 5, v2
	v_sub_u32_e32 v1, v1, v4
	v_add_u32_e32 v3, v5, v3
	v_and_b32_e32 v2, 32, v2
	v_ashrrev_i16_sdwa v1, v248, sext(v1) dst_sel:DWORD dst_unused:UNUSED_PAD src0_sel:DWORD src1_sel:BYTE_0
	v_add_u32_sdwa v1, v2, sext(v1) dst_sel:DWORD dst_unused:UNUSED_PAD src0_sel:DWORD src1_sel:WORD_0
	v_lshlrev_b32_e32 v2, 1, v3
	v_lshrrev_b32_e32 v4, 2, v3
	v_and_b32_e32 v5, 3, v5
	s_mov_b32 s4, 0xffffe0
	s_ashr_i32 s8, s7, 6
	v_and_b32_e32 v2, 24, v2
	v_and_b32_e32 v4, 4, v4
	v_and_or_b32 v5, v3, s4, v5
	v_or3_b32 v2, v5, v4, v2
	s_movk_i32 s4, 0x700
	s_lshl_b32 s29, s8, 10
	v_mul_lo_u32 v3, v3, s4
	v_mul_u32_u24_e32 v2, 0x700, v2
	s_add_i32 s30, s29, 0
	s_mov_b64 s[4:5], s[18:19]
	s_ashr_i32 s9, s7, 8
	v_add_lshl_u32 v112, v2, v1, 1
	s_add_i32 m0, s30, 0x10000
	v_add_lshl_u32 v154, v1, v3, 1
	global_load_lds_dwordx4 v112, s[4:5]
	s_add_u32 s4, s18, 0x38000
	s_addc_u32 s5, s19, 0
	s_add_i32 m0, s30, 0x12000
	s_nop 0
	global_load_lds_dwordx4 v112, s[4:5]
	s_add_u32 s4, s18, 0x70000
	s_addc_u32 s5, s19, 0
	s_add_i32 m0, s30, 0x14000
	s_nop 0
	global_load_lds_dwordx4 v112, s[4:5]
	s_add_u32 s4, s18, 0xa8000
	s_addc_u32 s5, s19, 0
	s_add_i32 m0, s30, 0x16000
	s_nop 0
	global_load_lds_dwordx4 v112, s[4:5]
	s_mov_b64 s[4:5], s[2:3]
	s_mov_b32 m0, s30
	s_nop 0
	global_load_lds_dwordx4 v154, s[4:5]
	s_add_u32 s4, s2, 0x38000
	s_addc_u32 s5, s3, 0
	s_add_i32 s31, s30, 0x2000
	s_mov_b32 m0, s31
	s_nop 0
	global_load_lds_dwordx4 v154, s[4:5]
	s_add_u32 s4, s2, 0x70000
	s_addc_u32 s5, s3, 0
	s_add_i32 s33, s30, 0x4000
	s_mov_b32 m0, s33
	s_nop 0
	global_load_lds_dwordx4 v154, s[4:5]
	s_add_u32 s4, s2, 0xa8000
	s_addc_u32 s5, s3, 0
	s_add_i32 s34, s30, 0x6000
	s_mov_b32 m0, s34
	s_cmp_eq_u32 s9, 1
	global_load_lds_dwordx4 v154, s[4:5]
	s_cselect_b64 s[4:5], -1, 0
	s_cmp_lg_u32 s9, 1
	s_cbranch_scc1 .LBB0_1827
	s_barrier
